# GEMM unit schedulers (P1, P7, P8): in-group index division by shift/mask when the group is full; v_rcp general division kept out of line as fallback
# speedup vs baseline: 1.0091x; 1.0091x over previous
.LBB0_119:
	v_cndmask_b32_e64 v2, 0, 1, s[58:59]
	v_cmp_ne_u32_e64 s[4:5], 1, v2
	s_andn2_b64 vcc, exec, s[58:59]
	s_mov_b64 s[44:45], 0
	s_cbranch_vccnz .LBB0_122
	s_add_i32 s2, s85, 2
	s_mul_i32 s7, s2, s33
	s_mul_hi_u32 s42, s2, s74
	s_add_i32 s7, s42, s7
	s_mul_i32 s2, s2, s74
	s_add_u32 s42, s2, s96
	s_addc_u32 s43, s7, s3
	v_cmp_gt_i64_e32 vcc, s[42:43], v[202:203]
	s_cbranch_vccnz .LBB0_122
	s_ashr_i32 s2, s42, 31
	s_lshr_b32 s2, s2, 29
	s_add_i32 s2, s42, s2
	s_ashr_i32 s7, s2, 3
	s_and_b32 s2, s2, -8
	s_sub_i32 s2, s42, s2
	s_cmp_lt_i32 s2, 0
	s_movk_i32 s42, 0x2e1
	s_cselect_b32 s42, s42, 0x2e0
	s_mul_i32 s2, s2, s42
	s_add_i32 s2, s2, s7
	s_mul_hi_i32 s7, s2, 0xb21642c9
	s_add_i32 s7, s7, s2
	s_lshr_b32 s42, s7, 31
	s_ashr_i32 s7, s7, 7
	s_add_i32 s7, s7, s42
	s_lshl_b32 s42, s7, 3
	s_sub_i32 s43, 0x100, s42
	s_min_i32 s43, s43, 8
	s_mulk_i32 s7, 0xff48
	s_add_i32 s7, s7, s2
	s_cmp_lg_u32 s43, 8
	s_cbranch_scc1 .Lq1_gen
	s_cmp_lt_i32 s7, 0
	s_cbranch_scc1 .Lq1_gen
	s_lshr_b32 s91, s7, 3
	s_and_b32 s2, s7, 7
.Lq1_join:
	s_add_i32 s92, s42, s2
	s_mov_b64 s[44:45], -1

.Lq1_gen:
	s_abs_i32 s44, s43
	v_cvt_f32_u32_e32 v2, s44
	s_sub_i32 s46, 0, s44
	v_rcp_iflag_f32_e32 v2, v2
	s_abs_i32 s2, s7
	s_xor_b32 s45, s7, s43
	s_ashr_i32 s45, s45, 31
	v_mul_f32_e32 v2, 0x4f7ffffe, v2
	v_cvt_u32_f32_e32 v2, v2
	s_nop 0
	v_readfirstlane_b32 s47, v2
	s_mul_i32 s46, s46, s47
	s_mul_hi_u32 s46, s47, s46
	s_add_i32 s47, s47, s46
	s_mul_hi_u32 s46, s2, s47
	s_mul_i32 s47, s46, s44
	s_sub_i32 s2, s2, s47
	s_add_i32 s48, s46, 1
	s_sub_i32 s47, s2, s44
	s_cmp_ge_u32 s2, s44
	s_cselect_b32 s46, s48, s46
	s_cselect_b32 s2, s47, s2
	s_add_i32 s47, s46, 1
	s_cmp_ge_u32 s2, s44
	s_cselect_b32 s2, s47, s46
	s_xor_b32 s2, s2, s45
	s_sub_i32 s91, s2, s45
	s_mul_i32 s2, s91, s43
	s_sub_i32 s2, s7, s2
	s_branch .Lq1_join

.LBB0_976:
	v_cndmask_b32_e64 v2, 0, 1, s[36:37]
	v_cmp_ne_u32_e64 s[4:5], 1, v2
	s_andn2_b64 vcc, exec, s[36:37]
	s_cbranch_vccnz .LBB0_981
	s_add_i32 s2, s67, 2
	s_mul_i32 s2, s2, s50
	s_add_i32 s2, s2, s9
	s_cmp_ge_i32 s2, s53
	s_mov_b64 s[28:29], 0
	s_cbranch_scc1 .LBB0_979
	s_ashr_i32 s11, s2, 31
	s_lshr_b32 s11, s11, 27
	s_add_i32 s11, s2, s11
	s_ashr_i32 s28, s11, 5
	s_lshl_b32 s28, s28, 2
	s_sub_i32 s29, s51, s28
	s_min_i32 s29, s29, 4
	s_andn2_b32 s11, s11, 31
	s_sub_i32 s2, s2, s11
	s_add_i32 s11, s28, s8
	s_cmp_lg_u32 s29, 4
	s_cbranch_scc1 .Lq7_gen
	s_cmp_lt_i32 s2, 0
	s_cbranch_scc1 .Lq7_gen
	s_lshr_b32 s28, s2, 2
	s_and_b32 s2, s2, 3
.Lq7_join:
	s_add_i32 s78, s11, s2
	s_lshl_b32 s2, s78, 2
	s_add_i32 s2, s2, 0
	s_add_i32 s2, s2, 0x21400
	v_mov_b32_e32 v2, s2
	ds_read_b32 v2, v2
	s_waitcnt lgkmcnt(0)
	v_readfirstlane_b32 s2, v2
	s_lshl_b32 s2, s2, 3
	s_add_i32 s79, s2, s28
	s_mov_b64 s[28:29], -1

.Lq7_gen:
	s_abs_i32 s30, s29
	v_cvt_f32_u32_e32 v2, s30
	s_sub_i32 s44, 0, s30
	v_rcp_iflag_f32_e32 v2, v2
	s_abs_i32 s28, s2
	s_xor_b32 s31, s2, s29
	v_mul_f32_e32 v2, 0x4f7ffffe, v2
	v_cvt_u32_f32_e32 v2, v2
	s_ashr_i32 s31, s31, 31
	v_readfirstlane_b32 s45, v2
	s_mul_i32 s44, s44, s45
	s_mul_hi_u32 s44, s45, s44
	s_add_i32 s45, s45, s44
	s_mul_hi_u32 s44, s28, s45
	s_mul_i32 s45, s44, s30
	s_sub_i32 s28, s28, s45
	s_add_i32 s46, s44, 1
	s_sub_i32 s45, s28, s30
	s_cmp_ge_u32 s28, s30
	s_cselect_b32 s44, s46, s44
	s_cselect_b32 s28, s45, s28
	s_add_i32 s45, s44, 1
	s_cmp_ge_u32 s28, s30
	s_cselect_b32 s28, s45, s44
	s_xor_b32 s28, s28, s31
	s_sub_i32 s28, s28, s31
	s_mul_i32 s29, s28, s29
	s_sub_i32 s2, s2, s29
	s_branch .Lq7_join

.LBB0_1077:
	v_cndmask_b32_e64 v2, 0, 1, s[0:1]
	v_cmp_ne_u32_e64 s[2:3], 1, v2
	s_andn2_b64 vcc, exec, s[0:1]
	s_mov_b64 s[10:11], 0
	s_cbranch_vccnz .LBB0_1080
	s_add_i32 s10, s24, 2
	s_mul_i32 s12, s10, s72
	s_add_i32 s12, s12, s33
	s_cmp_ge_i32 s12, s83
	s_mov_b64 s[10:11], 0
	s_cbranch_scc1 .LBB0_1080
	s_ashr_i32 s10, s12, 31
	s_lshr_b32 s10, s10, 27
	s_add_i32 s10, s12, s10
	s_ashr_i32 s11, s10, 5
	s_lshl_b32 s11, s11, 3
	s_sub_i32 s13, s9, s11
	s_min_i32 s13, s13, 8
	s_andn2_b32 s10, s10, 31
	s_sub_i32 s10, s12, s10
	s_add_i32 s11, s11, s88
	s_cmp_lg_u32 s13, 8
	s_cbranch_scc1 .Lq8_gen
	s_cmp_lt_i32 s10, 0
	s_cbranch_scc1 .Lq8_gen
	s_lshr_b32 s12, s10, 3
	s_and_b32 s10, s10, 7
.Lq8_join:
	s_add_i32 s25, s11, s10
	s_lshl_b32 s10, s25, 2
	s_add_i32 s10, s10, 0
	s_add_i32 s10, s10, 0x21400
	v_mov_b32_e32 v2, s10
	ds_read_b32 v2, v2
	s_waitcnt lgkmcnt(0)
	v_readfirstlane_b32 s10, v2
	s_lshl_b32 s10, s10, 2
	s_add_i32 s26, s10, s12
	s_mov_b64 s[10:11], -1

.Lq8_gen:
	s_abs_i32 s25, s13
	v_cvt_f32_u32_e32 v2, s25
	s_sub_i32 s28, 0, s25
	v_rcp_iflag_f32_e32 v2, v2
	s_abs_i32 s12, s10
	s_xor_b32 s26, s10, s13
	v_mul_f32_e32 v2, 0x4f7ffffe, v2
	v_cvt_u32_f32_e32 v2, v2
	s_ashr_i32 s26, s26, 31
	v_readfirstlane_b32 s29, v2
	s_mul_i32 s28, s28, s29
	s_mul_hi_u32 s28, s29, s28
	s_add_i32 s29, s29, s28
	s_mul_hi_u32 s28, s12, s29
	s_mul_i32 s29, s28, s25
	s_sub_i32 s12, s12, s29
	s_add_i32 s30, s28, 1
	s_sub_i32 s29, s12, s25
	s_cmp_ge_u32 s12, s25
	s_cselect_b32 s28, s30, s28
	s_cselect_b32 s12, s29, s12
	s_add_i32 s29, s28, 1
	s_cmp_ge_u32 s12, s25
	s_cselect_b32 s12, s29, s28
	s_xor_b32 s12, s12, s26
	s_sub_i32 s12, s12, s26
	s_mul_i32 s13, s12, s13
	s_sub_i32 s10, s10, s13
	s_branch .Lq8_join
